# prologue GEMV/transposes: items dealt by blockIdx*8+wave instead of vcu*8+wave so the 512 extra 128-KB GEMV items spread over all 8 XCDs
# speedup vs baseline: 1.0060x; 1.0060x over previous
; #define LAS __attribute__((address_space(3)))
; #define WS_FRESH() GAS unsigned char* wsg_ = (GAS unsigned char*)ws0; asm volatile("" : "+s"(wsg_)); unsigned char* ws = (unsigned char*)wsg_
; __global__ void __launch_bounds__(NWAVES * 64, 2) mk_fwd(Args args) {
;     ...
;         WS_FRESH();
;         LAS float* scr = (LAS float*)(lds + RING_OFF + wave * 16384);
;         constexpr int I_MOD = KSPLIT * DEPTH * 72, I_FFN = 5632, I_MQ = 32 * 192, I_MO = 32 * 64;
;         constexpr int NITEMS = I_MOD + 2 * I_FFN;
;         (void)I_MO; (void)I_MQ;
;         for (int it = gw; it < NITEMS; it += NGW) {
;             int r = it;
;             if (r < I_MOD) { p0_mod_item(c_in, ada_w, W_modp, r, lane); continue; } r -= I_MOD;
;             if (r < I_FFN) p0_transpose_item(w_gate, D, F, W_wgu, 1, 0, scr, r, lane);
;             else p0_transpose_item(w_up, D, F, W_wgu, 2, 0, scr, r - I_FFN, lane);
;         }
.LBB0_7:
	s_or_b64 exec, exec, s[0:1]
	v_readlane_b32 s0, v250, 2
	s_lshl_b32 s0, s0, 3
	s_lshr_b32 s94, s33, 6
	v_writelane_b32 v250, s0, 43
	v_and_b32_e32 v72, 63, v0
	v_lshrrev_b32_e32 v47, 3, v72
	v_writelane_b32 v250, s1, 44
	v_lshlrev_b32_e32 v46, 2, v72
	v_readlane_b32 s0, v250, 4
	s_lshl_b32 s0, s0, 3
	s_add_i32 s86, s0, s94
	v_readlane_b32 s0, v250, 37
	v_readlane_b32 s1, v250, 38
	v_readlane_b32 s2, v250, 39
	v_readlane_b32 s3, v250, 40
	s_mov_b64 s[0:1], s[2:3]
	s_lshl_b32 s2, s94, 14
	s_add_i32 s2, s2, 0
	v_writelane_b32 v250, s2, 45
	s_cmpk_gt_i32 s86, 0x3dff
	s_cbranch_scc1 .LBB0_20
	v_lshlrev_b32_e32 v4, 3, v0
	v_readlane_b32 s2, v250, 45
	v_and_b32_e32 v4, 56, v4
	v_lshrrev_b32_e32 v1, 5, v72
	v_and_b32_e32 v2, 31, v0
	v_mov_b32_e32 v49, 0
	s_mov_b32 s4, s2
	v_lshlrev_b32_e32 v48, 1, v4
	s_add_u32 s5, s0, 0x10000
	v_readlane_b32 s8, v250, 5
	v_lshl_add_u32 v3, v2, 2, s4
	v_mul_u32_u24_e32 v6, 0x84, v1
	v_mul_u32_u24_e32 v7, 0x84, v4
	v_lshl_add_u64 v[4:5], s[0:1], 0, v[48:49]
	s_mov_b64 s[2:3], 0x75c000
	s_addc_u32 s7, s1, 0
	v_readlane_b32 s9, v250, 6
	v_readlane_b32 s14, v250, 11
	v_lshl_add_u64 v[50:51], v[4:5], 0, s[2:3]
	v_lshlrev_b32_e32 v4, 2, v47
	v_readlane_b32 s11, v250, 8
	v_readlane_b32 s13, v250, 10
	v_readlane_b32 s15, v250, 12
	v_readlane_b32 s17, v250, 14
	v_readlane_b32 s19, v250, 16
	v_readlane_b32 s21, v250, 18
	v_readlane_b32 s23, v250, 20
	s_add_u32 s9, s14, 0x10e000
	v_add_u32_e32 v77, v3, v6
	v_add3_u32 v73, s4, v7, v4
	v_or_b32_e32 v74, 8, v47
	v_or_b32_e32 v75, 16, v47
	v_or_b32_e32 v76, 24, v47
	s_addc_u32 s11, s15, 0
	s_mov_b32 s1, 0
	s_mov_b32 s13, 0xb000
	s_mov_b32 s15, 0x16000
	s_mov_b32 s17, 0x21000
	s_mov_b32 s19, 0x2c000
	s_mov_b32 s21, 0x37000
	s_mov_b32 s23, 0x42000
	s_mov_b32 s24, 0x4d000
	s_mov_b32 s25, 0x58000
	s_mov_b32 s26, 0x63000
	s_mov_b32 s27, 0x6e000
	s_mov_b32 s28, 0x79000
	s_mov_b32 s29, 0x84000
	s_mov_b32 s30, 0x8f000
	s_mov_b32 s31, 0x9a000
	s_mov_b32 s34, 0xa5000
	s_mov_b32 s35, 0xb0000
	s_mov_b32 s36, 0xbb000
	s_mov_b32 s37, 0xc6000
	s_mov_b32 s38, 0xd1000
	s_mov_b32 s39, 0xdc000
	s_mov_b32 s40, 0xe7000
	s_mov_b32 s41, 0xf2000
	s_mov_b32 s42, 0xfd000
	s_mov_b32 s43, 0x108000
	s_mov_b32 s44, 0x113000
	s_mov_b32 s45, 0x11e000
	s_mov_b32 s46, 0x129000
	s_mov_b32 s47, 0x134000
	s_mov_b32 s48, 0x13f000
	s_mov_b32 s49, 0x14a000
	s_mov_b32 s50, 0x155000
	s_movk_i32 s51, 0x7fff
	s_mov_b32 s52, 0xffff0000
	v_lshlrev_b32_e32 v52, 2, v2
	v_add_u32_e32 v78, 0x400, v77
	v_add_u32_e32 v79, 0x800, v77
	v_add_u32_e32 v80, 0xc00, v77
	v_add_u32_e32 v81, 0x1000, v77
	v_add_u32_e32 v82, 0x1400, v77
	v_add_u32_e32 v83, 0x1800, v77
	v_add_u32_e32 v84, 0x1c00, v77
	v_readlane_b32 s53, v250, 3
	s_lshl_b32 s53, s53, 3
	s_add_i32 s53, s53, s94
	v_readlane_b32 s10, v250, 7
	v_readlane_b32 s12, v250, 9
	v_readlane_b32 s16, v250, 13
	v_readlane_b32 s18, v250, 15
	v_readlane_b32 s20, v250, 17
	v_readlane_b32 s22, v250, 19
	s_branch .LBB0_10
